# P2c: gate-stage and output-stage LDS reads requested as one batch (free VGPRs) instead of one round trip per element; plus the wait placement of v68
# speedup vs baseline: 1.0169x; 1.0022x over previous
; #define LAS __attribute__((address_space(3)))
; __device__ __forceinline__ float bf2f(bf16_t b) { return __uint_as_float(((unsigned)b) << 16); }
; __device__ __forceinline__ void hg_gate(float z, float lb, float& lf, float& kk) { const float f = lb + (1.0f - lb) * sigmoidf_(z); lf = __logf(f); kk = 1.0f - f; }
; __device__ __forceinline__ void hg_out_phase(const Params& p, Frame& F) {
;     ...
;         { const bf16_t* ST = (const bf16_t*)(ws + WS_SST) + (size_t)item * 16384;
; #pragma unroll
;           for (int nb = 0; nb < 4; ++nb)
; #pragma unroll
;               for (int ks = 0; ks < 4; ++ks) stf[nb][ks] = *(const bf16x8*)(ST + (size_t)(16 * (4 * vh + nb) + fr) * 128 + 32 * ks + 8 * fq); }
;         __builtin_amdgcn_sched_barrier(0);
;         const int k = tid & 127, tq = w >> 1;
;         const float lb = 1.0f / (1.0f + __expf(l1 - l0));
;         float cs[16], kk[16], rq[16]; float run = 0.f;
; #pragma unroll
;         for (int j = 0; j < 16; ++j) { float lf; hg_gate(bf2f(ZR[(16 * tq + j) * 128 + k]), lb, lf, kk[j]); run += lf; cs[j] = run; rq[j] = bf2f(QR[(16 * tq + j) * 128 + k]); }
;         seg[tq * 128 + k] = run;
;         { unsigned pk[8];
; #pragma unroll
;           for (int j = 0; j < 8; ++j) pk[j] = (unsigned)VR[(16 * tq + 2 * j) * 128 + k] | ((unsigned)VR[(16 * tq + 2 * j + 1) * 128 + k] << 16);
;           *(LAS u32x4*)(VT + k * TT + 16 * tq) = (u32x4){pk[0], pk[1], pk[2], pk[3]}; *(LAS u32x4*)(VT + k * TT + 16 * tq + 8) = (u32x4){pk[4], pk[5], pk[6], pk[7]}; }
.LBB0_572:
	s_ashr_i32 s91, s90, 31
	s_lshl_b64 s[0:1], s[90:91], 15
	v_lshl_add_u64 v[2:3], v[92:93], 0, s[0:1]
	v_lshl_add_u64 v[4:5], v[2:3], 0, v[98:99]
	global_load_dwordx4 v[30:33], v[4:5], off
	global_load_dwordx4 v[34:37], v[4:5], off offset:64
	global_load_dwordx4 v[38:41], v[4:5], off offset:128
	global_load_dwordx4 v[42:45], v[4:5], off offset:192
	v_lshl_add_u64 v[4:5], v[2:3], 0, v[100:101]
	global_load_dwordx4 v[46:49], v[4:5], off
	global_load_dwordx4 v[50:53], v[4:5], off offset:64
	global_load_dwordx4 v[54:57], v[4:5], off offset:128
	global_load_dwordx4 v[58:61], v[4:5], off offset:192
	v_lshl_add_u64 v[4:5], v[2:3], 0, v[102:103]
	v_lshl_add_u64 v[10:11], v[2:3], 0, v[104:105]
	global_load_dwordx4 v[62:65], v[4:5], off
	global_load_dwordx4 v[26:29], v[4:5], off offset:64
	global_load_dwordx4 v[22:25], v[4:5], off offset:128
	global_load_dwordx4 v[18:21], v[4:5], off offset:192
	global_load_dwordx4 v[14:17], v[10:11], off
	s_nop 0
	global_load_dwordx4 v[2:5], v[10:11], off offset:64
	global_load_dwordx4 v[6:9], v[10:11], off offset:128
	s_nop 0
	global_load_dwordx4 v[10:13], v[10:11], off offset:192
	s_mul_i32 s0, s61, 0xc000
	s_add_i32 s91, s0, 0
	v_sub_f32_e32 v66, v67, v66
	v_mul_f32_e32 v66, 0x3fb8aa3b, v66
	v_exp_f32_e32 v66, v66
	s_nop 0
	v_add_f32_e32 v66, 1.0, v66
	v_div_scale_f32 v67, s[0:1], v66, v66, 1.0
	v_rcp_f32_e32 v68, v67
	s_nop 0
	v_fma_f32 v69, -v67, v68, 1.0
	v_fmac_f32_e32 v68, v69, v68
	v_div_scale_f32 v69, vcc, 1.0, v66, 1.0
	v_mul_f32_e32 v70, v69, v68
	v_fma_f32 v71, -v67, v70, v69
	v_fmac_f32_e32 v70, v71, v68
	v_fma_f32 v67, -v67, v70, v69
	v_div_fmas_f32 v67, v67, v68, v70
	v_div_fixup_f32 v66, v67, v66, 1.0
	v_lshl_add_u32 v67, v89, 1, s91
	s_add_i32 s100, s91, s62
	v_lshl_add_u32 v246, v120, 1, s100
	ds_read_u16 v224, v67 offset:16384
	ds_read_u16 v225, v67 offset:16640
	ds_read_u16 v226, v67 offset:16896
	ds_read_u16 v227, v67 offset:17152
	ds_read_u16 v228, v67 offset:17408
	ds_read_u16 v229, v67 offset:17664
	ds_read_u16 v230, v67 offset:17920
	ds_read_u16 v231, v67 offset:18176
	ds_read_u16 v232, v67 offset:18432
	ds_read_u16 v233, v67 offset:18688
	ds_read_u16 v234, v67 offset:18944
	ds_read_u16 v235, v67 offset:19200
	ds_read_u16 v236, v67 offset:19456
	ds_read_u16 v237, v67 offset:19712
	ds_read_u16 v238, v67 offset:19968
	ds_read_u16 v239, v67 offset:20224
	ds_read_u16 v208, v246 offset:32768
	ds_read_u16 v209, v246 offset:33024
	ds_read_u16 v210, v246 offset:33280
	ds_read_u16 v211, v246 offset:33536
	ds_read_u16 v212, v246 offset:33792
	ds_read_u16 v213, v246 offset:34048
	ds_read_u16 v214, v246 offset:34304
	ds_read_u16 v215, v246 offset:34560
	ds_read_u16 v216, v246 offset:34816
	ds_read_u16 v217, v246 offset:35072
	ds_read_u16 v218, v246 offset:35328
	ds_read_u16 v219, v246 offset:35584
	ds_read_u16 v220, v246 offset:35840
	ds_read_u16 v221, v246 offset:36096
	ds_read_u16 v222, v246 offset:36352
	ds_read_u16 v223, v246 offset:36608
	v_sub_f32_e32 v75, 1.0, v66
	s_waitcnt lgkmcnt(0)
	v_mov_b32_e32 v68, v224
	v_lshlrev_b32_e32 v68, 16, v68
	v_mul_f32_e32 v68, 0xbfb8aa3b, v68
	v_exp_f32_e32 v68, v68
	s_nop 0
	v_add_f32_e32 v68, 1.0, v68
	v_rcp_f32_e32 v68, v68
	s_nop 0
	v_fma_f32 v69, v75, v68, v66
	v_cmp_gt_f32_e32 vcc, s69, v69
	s_nop 1
	v_cndmask_b32_e64 v68, 0, 32, vcc
	v_ldexp_f32 v68, v69, v68
	v_log_f32_e32 v68, v68
	s_nop 0
	v_mul_f32_e32 v70, 0x3f317217, v68
	v_fma_f32 v70, v68, s70, -v70
	v_fmac_f32_e32 v70, 0x3377d1cf, v68
	v_fmac_f32_e32 v70, 0x3f317217, v68
	v_cmp_lt_f32_e64 s[0:1], |v68|, s71
	s_nop 1
	v_cndmask_b32_e64 v68, v68, v70, s[0:1]
	v_cndmask_b32_e32 v70, 0, v163, vcc
	v_sub_f32_e32 v68, v68, v70
	ds_read_u16 v70, v67
	v_mov_b32_e32 v71, v225
	v_add_f32_e32 v68, 0, v68
	v_lshlrev_b32_e32 v71, 16, v71
	v_mul_f32_e32 v71, 0xbfb8aa3b, v71
	v_exp_f32_e32 v71, v71
	s_nop 0
	v_add_f32_e32 v71, 1.0, v71
	v_rcp_f32_e32 v71, v71
	s_nop 0
	v_fma_f32 v72, v75, v71, v66
	v_cmp_gt_f32_e32 vcc, s69, v72
	s_nop 1
	v_cndmask_b32_e64 v71, 0, 32, vcc
	v_ldexp_f32 v71, v72, v71
	v_log_f32_e32 v71, v71
	s_nop 0
	v_mul_f32_e32 v73, 0x3f317217, v71
	v_fma_f32 v73, v71, s70, -v73
	v_fmac_f32_e32 v73, 0x3377d1cf, v71
	v_fmac_f32_e32 v73, 0x3f317217, v71
	v_cmp_lt_f32_e64 s[0:1], |v71|, s71
	s_nop 1
	v_cndmask_b32_e64 v71, v71, v73, s[0:1]
	v_cndmask_b32_e32 v73, 0, v163, vcc
	v_sub_f32_e32 v71, v71, v73
	ds_read_u16 v73, v67 offset:256
	v_mov_b32_e32 v74, v226
	v_add_f32_e32 v71, v68, v71
	v_lshlrev_b32_e32 v74, 16, v74
	v_mul_f32_e32 v74, 0xbfb8aa3b, v74
	v_exp_f32_e32 v74, v74
	s_nop 0
	v_add_f32_e32 v74, 1.0, v74
	v_rcp_f32_e32 v74, v74
	s_nop 0
	v_fma_f32 v76, v75, v74, v66
	v_cmp_gt_f32_e32 vcc, s69, v76
	s_nop 1
	v_cndmask_b32_e64 v74, 0, 32, vcc
	v_ldexp_f32 v74, v76, v74
	v_log_f32_e32 v74, v74
	s_nop 0
	v_mul_f32_e32 v77, 0x3f317217, v74
	v_fma_f32 v77, v74, s70, -v77
	v_fmac_f32_e32 v77, 0x3377d1cf, v74
	v_fmac_f32_e32 v77, 0x3f317217, v74
	v_cmp_lt_f32_e64 s[0:1], |v74|, s71
	s_nop 1
	v_cndmask_b32_e64 v74, v74, v77, s[0:1]
	v_cndmask_b32_e32 v77, 0, v163, vcc
	v_sub_f32_e32 v74, v74, v77
	ds_read_u16 v77, v67 offset:512
	v_mov_b32_e32 v78, v227
	v_add_f32_e32 v74, v71, v74
	v_lshlrev_b32_e32 v78, 16, v78
	v_mul_f32_e32 v78, 0xbfb8aa3b, v78
	v_exp_f32_e32 v78, v78
	s_nop 0
	v_add_f32_e32 v78, 1.0, v78
	v_rcp_f32_e32 v78, v78
	s_nop 0
	v_fma_f32 v79, v75, v78, v66
	v_cmp_gt_f32_e32 vcc, s69, v79
	s_nop 1
	v_cndmask_b32_e64 v78, 0, 32, vcc
	v_ldexp_f32 v78, v79, v78
	v_log_f32_e32 v78, v78
	s_nop 0
	v_mul_f32_e32 v80, 0x3f317217, v78
	v_fma_f32 v80, v78, s70, -v80
	v_fmac_f32_e32 v80, 0x3377d1cf, v78
	v_fmac_f32_e32 v80, 0x3f317217, v78
	v_cmp_lt_f32_e64 s[0:1], |v78|, s71
; __device__ __forceinline__ float bf2f(bf16_t b) { return __uint_as_float(((unsigned)b) << 16); }
; __device__ __forceinline__ void hg_gate(float z, float lb, float& lf, float& kk) { const float f = lb + (1.0f - lb) * sigmoidf_(z); lf = __logf(f); kk = 1.0f - f; }
; __device__ __forceinline__ void hg_out_phase(const Params& p, Frame& F) {
;     ...
;         const float lb = 1.0f / (1.0f + __expf(l1 - l0));
;         float cs[16], kk[16], rq[16]; float run = 0.f;
; #pragma unroll
;         for (int j = 0; j < 16; ++j) { float lf; hg_gate(bf2f(ZR[(16 * tq + j) * 128 + k]), lb, lf, kk[j]); run += lf; cs[j] = run; rq[j] = bf2f(QR[(16 * tq + j) * 128 + k]); }
	s_nop 1
	v_cndmask_b32_e64 v78, v78, v80, s[0:1]
	v_cndmask_b32_e32 v80, 0, v163, vcc
	v_sub_f32_e32 v78, v78, v80
	ds_read_u16 v81, v67 offset:768
	v_mov_b32_e32 v80, v228
	v_add_f32_e32 v78, v74, v78
	v_lshlrev_b32_e32 v80, 16, v80
	v_mul_f32_e32 v80, 0xbfb8aa3b, v80
	v_exp_f32_e32 v80, v80
	s_nop 0
	v_add_f32_e32 v80, 1.0, v80
	v_rcp_f32_e32 v80, v80
	s_nop 0
	v_fma_f32 v83, v75, v80, v66
	v_cmp_gt_f32_e32 vcc, s69, v83
	s_nop 1
	v_cndmask_b32_e64 v80, 0, 32, vcc
	v_ldexp_f32 v80, v83, v80
	v_log_f32_e32 v80, v80
	s_nop 0
	v_mul_f32_e32 v82, 0x3f317217, v80
	v_fma_f32 v82, v80, s70, -v82
	v_fmac_f32_e32 v82, 0x3377d1cf, v80
	v_fmac_f32_e32 v82, 0x3f317217, v80
	v_cmp_lt_f32_e64 s[0:1], |v80|, s71
	s_nop 1
	v_cndmask_b32_e64 v80, v80, v82, s[0:1]
	v_cndmask_b32_e32 v82, 0, v163, vcc
	v_sub_f32_e32 v80, v80, v82
	ds_read_u16 v84, v67 offset:1024
	v_mov_b32_e32 v82, v229
	v_add_f32_e32 v80, v78, v80
	v_lshlrev_b32_e32 v82, 16, v82
	v_mul_f32_e32 v82, 0xbfb8aa3b, v82
	v_exp_f32_e32 v82, v82
	s_nop 0
	v_add_f32_e32 v82, 1.0, v82
	v_rcp_f32_e32 v82, v82
	s_nop 0
	v_fma_f32 v86, v75, v82, v66
	v_cmp_gt_f32_e32 vcc, s69, v86
	s_nop 1
	v_cndmask_b32_e64 v82, 0, 32, vcc
	v_ldexp_f32 v82, v86, v82
	v_log_f32_e32 v82, v82
	s_nop 0
	v_mul_f32_e32 v85, 0x3f317217, v82
	v_fma_f32 v85, v82, s70, -v85
	v_fmac_f32_e32 v85, 0x3377d1cf, v82
	v_fmac_f32_e32 v85, 0x3f317217, v82
	v_cmp_lt_f32_e64 s[0:1], |v82|, s71
	s_nop 1
	v_cndmask_b32_e64 v82, v82, v85, s[0:1]
	v_cndmask_b32_e32 v85, 0, v163, vcc
	v_sub_f32_e32 v82, v82, v85
	ds_read_u16 v87, v67 offset:1280
	v_mov_b32_e32 v85, v230
	v_add_f32_e32 v82, v80, v82
	v_lshlrev_b32_e32 v85, 16, v85
	v_mul_f32_e32 v85, 0xbfb8aa3b, v85
	v_exp_f32_e32 v85, v85
	s_nop 0
	v_add_f32_e32 v85, 1.0, v85
	v_rcp_f32_e32 v85, v85
	s_nop 0
	v_fma_f32 v171, v75, v85, v66
	v_cmp_gt_f32_e32 vcc, s69, v171
	s_nop 1
	v_cndmask_b32_e64 v85, 0, 32, vcc
	v_ldexp_f32 v85, v171, v85
	v_log_f32_e32 v85, v85
	s_nop 0
	v_mul_f32_e32 v172, 0x3f317217, v85
	v_fma_f32 v172, v85, s70, -v172
	v_fmac_f32_e32 v172, 0x3377d1cf, v85
	v_fmac_f32_e32 v172, 0x3f317217, v85
	v_cmp_lt_f32_e64 s[0:1], |v85|, s71
	s_nop 1
	v_cndmask_b32_e64 v85, v85, v172, s[0:1]
	v_cndmask_b32_e32 v172, 0, v163, vcc
	v_sub_f32_e32 v85, v85, v172
	ds_read_u16 v172, v67 offset:1536
	v_mov_b32_e32 v173, v231
	v_add_f32_e32 v85, v82, v85
	v_lshlrev_b32_e32 v173, 16, v173
	v_mul_f32_e32 v173, 0xbfb8aa3b, v173
	v_exp_f32_e32 v173, v173
	s_nop 0
	v_add_f32_e32 v173, 1.0, v173
	v_rcp_f32_e32 v173, v173
	s_nop 0
	v_fma_f32 v176, v75, v173, v66
	v_cmp_gt_f32_e32 vcc, s69, v176
	s_nop 1
	v_cndmask_b32_e64 v173, 0, 32, vcc
	v_ldexp_f32 v173, v176, v173
	v_log_f32_e32 v173, v173
	s_nop 0
	v_mul_f32_e32 v174, 0x3f317217, v173
	v_fma_f32 v174, v173, s70, -v174
	v_fmac_f32_e32 v174, 0x3377d1cf, v173
	v_fmac_f32_e32 v174, 0x3f317217, v173
	v_cmp_lt_f32_e64 s[0:1], |v173|, s71
	s_nop 1
	v_cndmask_b32_e64 v173, v173, v174, s[0:1]
	v_cndmask_b32_e32 v174, 0, v163, vcc
	v_sub_f32_e32 v173, v173, v174
	ds_read_u16 v177, v67 offset:1792
	v_mov_b32_e32 v174, v232
	v_add_f32_e32 v173, v85, v173
	v_lshlrev_b32_e32 v174, 16, v174
	v_mul_f32_e32 v174, 0xbfb8aa3b, v174
	v_exp_f32_e32 v174, v174
	s_nop 0
	v_add_f32_e32 v174, 1.0, v174
	v_rcp_f32_e32 v174, v174
	s_nop 0
	v_fma_f32 v178, v75, v174, v66
	v_cmp_gt_f32_e32 vcc, s69, v178
	s_nop 1
	v_cndmask_b32_e64 v174, 0, 32, vcc
	v_ldexp_f32 v174, v178, v174
	v_log_f32_e32 v174, v174
	s_nop 0
	v_mul_f32_e32 v175, 0x3f317217, v174
	v_fma_f32 v175, v174, s70, -v175
	v_fmac_f32_e32 v175, 0x3377d1cf, v174
	v_fmac_f32_e32 v175, 0x3f317217, v174
	v_cmp_lt_f32_e64 s[0:1], |v174|, s71
	s_nop 1
	v_cndmask_b32_e64 v174, v174, v175, s[0:1]
	v_cndmask_b32_e32 v175, 0, v163, vcc
	v_sub_f32_e32 v174, v174, v175
	ds_read_u16 v179, v67 offset:2048
	v_mov_b32_e32 v175, v233
	v_add_f32_e32 v174, v173, v174
	v_lshlrev_b32_e32 v175, 16, v175
	v_mul_f32_e32 v175, 0xbfb8aa3b, v175
	v_exp_f32_e32 v175, v175
	s_nop 0
	v_add_f32_e32 v175, 1.0, v175
	v_rcp_f32_e32 v175, v175
	s_nop 0
	v_fma_f32 v181, v75, v175, v66
	v_cmp_gt_f32_e32 vcc, s69, v181
	s_nop 1
	v_cndmask_b32_e64 v175, 0, 32, vcc
	v_ldexp_f32 v175, v181, v175
	v_log_f32_e32 v175, v175
	s_nop 0
	v_mul_f32_e32 v180, 0x3f317217, v175
	v_fma_f32 v180, v175, s70, -v180
	v_fmac_f32_e32 v180, 0x3377d1cf, v175
	v_fmac_f32_e32 v180, 0x3f317217, v175
	v_cmp_lt_f32_e64 s[0:1], |v175|, s71
	s_nop 1
	v_cndmask_b32_e64 v175, v175, v180, s[0:1]
	v_cndmask_b32_e32 v180, 0, v163, vcc
	v_sub_f32_e32 v175, v175, v180
	ds_read_u16 v183, v67 offset:2304
	v_mov_b32_e32 v180, v234
	v_add_f32_e32 v175, v174, v175
	v_lshlrev_b32_e32 v180, 16, v180
	v_mul_f32_e32 v180, 0xbfb8aa3b, v180
	v_exp_f32_e32 v180, v180
	s_nop 0
	v_add_f32_e32 v180, 1.0, v180
	v_rcp_f32_e32 v180, v180
	s_nop 0
	v_fma_f32 v185, v75, v180, v66
	v_cmp_gt_f32_e32 vcc, s69, v185
; #define LAS __attribute__((address_space(3)))
; __device__ __forceinline__ float bf2f(bf16_t b) { return __uint_as_float(((unsigned)b) << 16); }
; #define LBAR() do { asm volatile("s_waitcnt lgkmcnt(0)" ::: "memory"); __builtin_amdgcn_s_barrier(); asm volatile("" ::: "memory"); } while (0)
; __device__ __forceinline__ void hg_gate(float z, float lb, float& lf, float& kk) { const float f = lb + (1.0f - lb) * sigmoidf_(z); lf = __logf(f); kk = 1.0f - f; }
; __device__ __forceinline__ void hg_out_phase(const Params& p, Frame& F) {
;     ...
;         for (int j = 0; j < 16; ++j) { float lf; hg_gate(bf2f(ZR[(16 * tq + j) * 128 + k]), lb, lf, kk[j]); run += lf; cs[j] = run; rq[j] = bf2f(QR[(16 * tq + j) * 128 + k]); }
;         seg[tq * 128 + k] = run;
;         { unsigned pk[8];
; #pragma unroll
;           for (int j = 0; j < 8; ++j) pk[j] = (unsigned)VR[(16 * tq + 2 * j) * 128 + k] | ((unsigned)VR[(16 * tq + 2 * j + 1) * 128 + k] << 16);
;           *(LAS u32x4*)(VT + k * TT + 16 * tq) = (u32x4){pk[0], pk[1], pk[2], pk[3]}; *(LAS u32x4*)(VT + k * TT + 16 * tq + 8) = (u32x4){pk[4], pk[5], pk[6], pk[7]}; }
;         LBAR();
	s_nop 1
	v_cndmask_b32_e64 v180, 0, 32, vcc
	v_ldexp_f32 v180, v185, v180
	v_log_f32_e32 v180, v180
	s_nop 0
	v_mul_f32_e32 v182, 0x3f317217, v180
	v_fma_f32 v182, v180, s70, -v182
	v_fmac_f32_e32 v182, 0x3377d1cf, v180
	v_fmac_f32_e32 v182, 0x3f317217, v180
	v_cmp_lt_f32_e64 s[0:1], |v180|, s71
	s_nop 1
	v_cndmask_b32_e64 v180, v180, v182, s[0:1]
	v_cndmask_b32_e32 v182, 0, v163, vcc
	v_sub_f32_e32 v180, v180, v182
	ds_read_u16 v186, v67 offset:2560
	v_mov_b32_e32 v182, v235
	v_add_f32_e32 v180, v175, v180
	v_lshlrev_b32_e32 v182, 16, v182
	v_mul_f32_e32 v182, 0xbfb8aa3b, v182
	v_exp_f32_e32 v182, v182
	s_nop 0
	v_add_f32_e32 v182, 1.0, v182
	v_rcp_f32_e32 v182, v182
	s_nop 0
	v_fma_f32 v188, v75, v182, v66
	v_cmp_gt_f32_e32 vcc, s69, v188
	s_nop 1
	v_cndmask_b32_e64 v182, 0, 32, vcc
	v_ldexp_f32 v182, v188, v182
	v_log_f32_e32 v182, v182
	s_nop 0
	v_mul_f32_e32 v184, 0x3f317217, v182
	v_fma_f32 v184, v182, s70, -v184
	v_fmac_f32_e32 v184, 0x3377d1cf, v182
	v_fmac_f32_e32 v184, 0x3f317217, v182
	v_cmp_lt_f32_e64 s[0:1], |v182|, s71
	s_nop 1
	v_cndmask_b32_e64 v182, v182, v184, s[0:1]
	v_cndmask_b32_e32 v184, 0, v163, vcc
	v_sub_f32_e32 v182, v182, v184
	ds_read_u16 v189, v67 offset:2816
	v_mov_b32_e32 v184, v236
	v_add_f32_e32 v182, v180, v182
	v_lshlrev_b32_e32 v184, 16, v184
	v_mul_f32_e32 v184, 0xbfb8aa3b, v184
	v_exp_f32_e32 v184, v184
	s_nop 0
	v_add_f32_e32 v184, 1.0, v184
	v_rcp_f32_e32 v184, v184
	s_nop 0
	v_fma_f32 v191, v75, v184, v66
	v_cmp_gt_f32_e32 vcc, s69, v191
	s_nop 1
	v_cndmask_b32_e64 v184, 0, 32, vcc
	v_ldexp_f32 v184, v191, v184
	v_log_f32_e32 v184, v184
	s_nop 0
	v_mul_f32_e32 v187, 0x3f317217, v184
	v_fma_f32 v187, v184, s70, -v187
	v_fmac_f32_e32 v187, 0x3377d1cf, v184
	v_fmac_f32_e32 v187, 0x3f317217, v184
	v_cmp_lt_f32_e64 s[0:1], |v184|, s71
	s_nop 1
	v_cndmask_b32_e64 v184, v184, v187, s[0:1]
	v_cndmask_b32_e32 v187, 0, v163, vcc
	v_sub_f32_e32 v184, v184, v187
	ds_read_u16 v192, v67 offset:3072
	v_mov_b32_e32 v187, v237
	v_add_f32_e32 v184, v182, v184
	v_lshlrev_b32_e32 v187, 16, v187
	v_mul_f32_e32 v187, 0xbfb8aa3b, v187
	v_exp_f32_e32 v187, v187
	s_nop 0
	v_add_f32_e32 v187, 1.0, v187
	v_rcp_f32_e32 v187, v187
	s_nop 0
	v_fma_f32 v193, v75, v187, v66
	v_cmp_gt_f32_e32 vcc, s69, v193
	s_nop 1
	v_cndmask_b32_e64 v187, 0, 32, vcc
	v_ldexp_f32 v187, v193, v187
	v_log_f32_e32 v187, v187
	s_nop 0
	v_mul_f32_e32 v190, 0x3f317217, v187
	v_fma_f32 v190, v187, s70, -v190
	v_fmac_f32_e32 v190, 0x3377d1cf, v187
	v_fmac_f32_e32 v190, 0x3f317217, v187
	v_cmp_lt_f32_e64 s[0:1], |v187|, s71
	s_nop 1
	v_cndmask_b32_e64 v187, v187, v190, s[0:1]
	v_cndmask_b32_e32 v190, 0, v163, vcc
	v_sub_f32_e32 v187, v187, v190
	ds_read_u16 v194, v67 offset:3328
	v_mov_b32_e32 v190, v238
	v_add_f32_e32 v187, v184, v187
	v_lshlrev_b32_e32 v190, 16, v190
	v_mul_f32_e32 v190, 0xbfb8aa3b, v190
	v_exp_f32_e32 v190, v190
	s_nop 0
	v_add_f32_e32 v190, 1.0, v190
	v_rcp_f32_e32 v190, v190
	s_nop 0
	v_fma_f32 v195, v75, v190, v66
	v_cmp_gt_f32_e32 vcc, s69, v195
	s_nop 1
	v_cndmask_b32_e64 v190, 0, 32, vcc
	v_ldexp_f32 v190, v195, v190
	v_log_f32_e32 v190, v190
	s_nop 0
	v_mul_f32_e32 v196, 0x3f317217, v190
	v_fma_f32 v196, v190, s70, -v196
	v_fmac_f32_e32 v196, 0x3377d1cf, v190
	v_fmac_f32_e32 v196, 0x3f317217, v190
	v_cmp_lt_f32_e64 s[0:1], |v190|, s71
	s_nop 1
	v_cndmask_b32_e64 v190, v190, v196, s[0:1]
	v_cndmask_b32_e32 v196, 0, v163, vcc
	v_sub_f32_e32 v190, v190, v196
	ds_read_u16 v196, v67 offset:3584
	v_mov_b32_e32 v197, v239
	v_add_f32_e32 v190, v187, v190
	ds_read_u16 v198, v67 offset:3840
	v_lshlrev_b32_e32 v197, 16, v197
	v_mul_f32_e32 v197, 0xbfb8aa3b, v197
	v_exp_f32_e32 v197, v197
	s_nop 0
	v_add_f32_e32 v197, 1.0, v197
	v_rcp_f32_e32 v197, v197
	s_nop 0
	v_fmac_f32_e32 v66, v75, v197
	v_cmp_gt_f32_e32 vcc, s69, v66
	s_nop 1
	v_cndmask_b32_e64 v75, 0, 32, vcc
	v_ldexp_f32 v75, v66, v75
	v_log_f32_e32 v75, v75
	s_nop 0
	v_mul_f32_e32 v197, 0x3f317217, v75
	v_fma_f32 v197, v75, s70, -v197
	v_fmac_f32_e32 v197, 0x3377d1cf, v75
	v_fmac_f32_e32 v197, 0x3f317217, v75
	v_cmp_lt_f32_e64 s[0:1], |v75|, s71
	s_nop 1
	v_cndmask_b32_e64 v75, v75, v197, s[0:1]
	v_cndmask_b32_e32 v197, 0, v163, vcc
	v_sub_f32_e32 v75, v75, v197
	v_add_f32_e32 v75, v190, v75
	s_add_i32 s0, s91, s62
	ds_write_b32 v121, v75
	v_lshl_add_u32 v197, v120, 1, s0
	s_andn2_b64 vcc, exec, s[74:75]
	v_lshl_or_b32 v200, v209, 16, v208
	v_lshl_or_b32 v201, v211, 16, v210
	v_lshl_or_b32 v202, v213, 16, v212
	v_lshl_or_b32 v203, v215, 16, v214
	v_lshl_or_b32 v204, v217, 16, v216
	v_lshl_or_b32 v205, v219, 16, v218
	v_lshl_or_b32 v206, v221, 16, v220
	v_lshl_or_b32 v207, v223, 16, v222
	ds_write_b128 v153, v[200:203]
	ds_write_b128 v153, v[204:207] offset:16
	s_waitcnt lgkmcnt(0)
	s_barrier
	v_mov_b32_e32 v197, 0
	s_cbranch_vccz .LBB0_583
	s_andn2_b64 vcc, exec, s[44:45]
	s_cbranch_vccz .LBB0_584

; __device__ __forceinline__ float bf2f(bf16_t b) { return __uint_as_float(((unsigned)b) << 16); }
; __device__ __forceinline__ float sigmoidf_(float x) { return __builtin_amdgcn_rcpf(1.0f + __expf(-x)); }
; __device__ __forceinline__ bf16_t f2bf(float v) { return (bf16_t)(cvt_pk_bf16(v, 0.f) & 0xffffu); }
; __device__ __forceinline__ void ml_out_phase(const Params& p, Frame& F) {
;     ...
; #pragma unroll
;         for (int i = 0; i < 4; ++i) { const int tl = 16 * tb + 4 * fq + i; const float r = 1.0f / sqrtf((ssqp[tl] + ssqp[64 + tl]) * (1.0f / 256.0f) + EPS);
; #pragma unroll
;             for (int nb = 0; nb < 8; ++nb) { const int v = 16 * (8 * vh + nb) + fr; const float g = bf2f(VR[tl * 256 + v]);
;                 VR[tl * 256 + v] = f2bf(o[nb][i] * r * nwl[v] * sigmoidf_(g)); } }
.LBB0_635:
	ds_read_u16 v54, v203 offset:34816
	ds_read_u16 v55, v203 offset:34848
	ds_read_b32 v56, v204
	ds_read_b32 v57, v205
	ds_read_u16 v58, v203 offset:34880
	ds_read_b32 v59, v206
	ds_read_u16 v60, v203 offset:34912
	ds_read_b32 v61, v207
	ds_read_u16 v62, v203 offset:34944
	ds_read_b32 v63, v208
	ds_read_u16 v64, v203 offset:34976
	ds_read_b32 v65, v209
	ds_read_u16 v66, v203 offset:35008
	ds_read_b32 v67, v210
	ds_read_u16 v68, v203 offset:35040
	ds_read_b32 v69, v211
	ds_read_u16 v70, v212 offset:34816
	ds_read_u16 v71, v212 offset:34848
	ds_read_u16 v72, v212 offset:34880
	ds_read_u16 v73, v212 offset:34912
	ds_read_u16 v74, v212 offset:34944
	ds_read_u16 v75, v212 offset:34976
	ds_read_u16 v76, v212 offset:35008
	ds_read_u16 v77, v212 offset:35040
	ds_read_u16 v78, v213 offset:34816
	ds_read_u16 v79, v213 offset:34848
	ds_read_u16 v80, v213 offset:34880
	ds_read_u16 v81, v213 offset:34912
	ds_read_u16 v82, v213 offset:34944
	ds_read_u16 v83, v213 offset:34976
	ds_read_u16 v84, v213 offset:35008
	ds_read_u16 v85, v213 offset:35040
	ds_read_u16 v86, v214 offset:34816
	ds_read_u16 v87, v214 offset:34848
	ds_read_u16 v88, v214 offset:34880
	ds_read_u16 v89, v214 offset:34912
	ds_read_u16 v90, v214 offset:34944
	ds_read_u16 v91, v214 offset:34976
	ds_read_u16 v92, v214 offset:35008
	ds_read_u16 v93, v214 offset:35040
	ds_read_b128 v[2:5], v202
	s_waitcnt lgkmcnt(0)
	ds_read_b128 v[6:9], v202 offset:256
	s_lshl_b32 s58, s58, 18
	s_waitcnt lgkmcnt(0)
	v_add_f32_e32 v2, v2, v6
	v_fmamk_f32 v2, v2, 0x3b800000, v221
	v_cmp_gt_f32_e32 vcc, s11, v2
	v_mul_f32_e32 v6, 0x4f800000, v2
	v_add_f32_e32 v3, v3, v7
	v_cndmask_b32_e32 v2, v2, v6, vcc
	v_sqrt_f32_e32 v6, v2
	v_fmamk_f32 v3, v3, 0x3b800000, v221
	v_mul_f32_e32 v7, 0x4f800000, v3
	v_add_u32_e32 v20, -1, v6
	v_fma_f32 v21, -v20, v6, v2
	v_cmp_ge_f32_e64 s[0:1], 0, v21
	v_add_u32_e32 v21, 1, v6
	s_nop 0
	v_cndmask_b32_e64 v20, v6, v20, s[0:1]
	v_fma_f32 v6, -v21, v6, v2
	v_cmp_lt_f32_e64 s[0:1], 0, v6
	s_nop 1
	v_cndmask_b32_e64 v6, v20, v21, s[0:1]
	v_mul_f32_e32 v20, 0x37800000, v6
	v_cndmask_b32_e32 v6, v6, v20, vcc
	v_cmp_class_f32_e32 vcc, v2, v222
	s_nop 1
	v_cndmask_b32_e32 v2, v6, v2, vcc
	v_div_scale_f32 v6, s[0:1], v2, v2, 1.0
	v_rcp_f32_e32 v20, v6
	s_nop 0
	v_fma_f32 v21, -v6, v20, 1.0
	v_fmac_f32_e32 v20, v21, v20
	v_div_scale_f32 v21, vcc, 1.0, v2, 1.0
	v_mul_f32_e32 v24, v21, v20
	v_fma_f32 v25, -v6, v24, v21
	v_fmac_f32_e32 v24, v25, v20
	v_fma_f32 v6, -v6, v24, v21
	v_div_fmas_f32 v6, v6, v20, v24
	v_div_fixup_f32 v2, v6, v2, 1.0
	v_mov_b32_e32 v6, v54
	v_mov_b32_e32 v21, v55
	v_mov_b32_e32 v20, v56
	v_mul_f32_e32 v24, v48, v2
	v_mul_f32_e32 v25, v44, v2
	v_lshlrev_b32_e32 v6, 16, v6
	v_mul_f32_e32 v6, 0xbfb8aa3b, v6
	v_exp_f32_e32 v6, v6
	v_lshlrev_b32_e32 v21, 16, v21
	v_mul_f32_e32 v21, 0xbfb8aa3b, v21
	v_mul_f32_e32 v24, v20, v24
	v_add_f32_e32 v6, 1.0, v6
	v_rcp_f32_e32 v6, v6
	v_exp_f32_e32 v21, v21
	v_mul_f32_e32 v28, v42, v2
	v_mul_f32_e32 v29, v40, v2
	v_mul_f32_e32 v6, v24, v6
	v_cvt_pk_bf16_f32 v6, v6, s0
	ds_write_b16 v203, v6 offset:34816
	v_mov_b32_e32 v6, v57
	v_add_f32_e32 v21, 1.0, v21
	v_rcp_f32_e32 v21, v21
	v_mul_f32_e32 v24, v46, v2
	v_mul_f32_e32 v32, v38, v2
	v_mul_f32_e32 v24, v6, v24
	v_mul_f32_e32 v21, v24, v21
	v_cvt_pk_bf16_f32 v21, v21, s0
	ds_write_b16 v203, v21 offset:34848
	v_mov_b32_e32 v21, v58
	v_mul_f32_e32 v33, v36, v2
	v_cmp_gt_f32_e32 vcc, s11, v3
	v_lshlrev_b32_e32 v24, 16, v21
	v_mul_f32_e32 v24, 0xbfb8aa3b, v24
	v_exp_f32_e32 v24, v24
	v_mov_b32_e32 v21, v59
	v_cndmask_b32_e32 v3, v3, v7, vcc
	v_sqrt_f32_e32 v7, v3
	v_add_f32_e32 v24, 1.0, v24
	v_rcp_f32_e32 v24, v24
	v_mul_f32_e32 v25, v25, v21
	v_mul_f32_e32 v24, v25, v24
	v_cvt_pk_bf16_f32 v24, v24, s0
	ds_write_b16 v203, v24 offset:34880
	v_mov_b32_e32 v24, v60
	v_lshlrev_b32_e32 v25, 16, v24
	v_mul_f32_e32 v25, 0xbfb8aa3b, v25
	v_exp_f32_e32 v25, v25
	v_mov_b32_e32 v24, v61
	v_add_f32_e32 v25, 1.0, v25
	v_rcp_f32_e32 v25, v25
	v_mul_f32_e32 v28, v28, v24
	v_mul_f32_e32 v25, v28, v25
	v_cvt_pk_bf16_f32 v25, v25, s0
	ds_write_b16 v203, v25 offset:34912
	v_mov_b32_e32 v25, v62
	v_lshlrev_b32_e32 v28, 16, v25
	v_mul_f32_e32 v28, 0xbfb8aa3b, v28
	v_exp_f32_e32 v28, v28
	v_mov_b32_e32 v25, v63
	v_add_f32_e32 v28, 1.0, v28
	v_rcp_f32_e32 v28, v28
	v_mul_f32_e32 v29, v29, v25
	v_mul_f32_e32 v28, v29, v28
	v_cvt_pk_bf16_f32 v28, v28, s0
	ds_write_b16 v203, v28 offset:34944
	v_mov_b32_e32 v28, v64
	v_lshlrev_b32_e32 v29, 16, v28
	v_mul_f32_e32 v29, 0xbfb8aa3b, v29
	v_exp_f32_e32 v29, v29
	v_mov_b32_e32 v28, v65
	v_add_f32_e32 v29, 1.0, v29
	v_rcp_f32_e32 v29, v29
	v_mul_f32_e32 v32, v32, v28
	v_mul_f32_e32 v29, v32, v29
	v_cvt_pk_bf16_f32 v29, v29, s0
	ds_write_b16 v203, v29 offset:34976
	v_mov_b32_e32 v29, v66
	v_lshlrev_b32_e32 v32, 16, v29
	v_mul_f32_e32 v32, 0xbfb8aa3b, v32
	v_exp_f32_e32 v32, v32
	v_mov_b32_e32 v29, v67
	v_add_f32_e32 v32, 1.0, v32
	v_rcp_f32_e32 v32, v32
	v_mul_f32_e32 v33, v33, v29
	v_mul_f32_e32 v32, v33, v32
	v_cvt_pk_bf16_f32 v32, v32, s0
	ds_write_b16 v203, v32 offset:35008
	v_mov_b32_e32 v32, v68
	v_mul_f32_e32 v33, v34, v2
	v_mov_b32_e32 v2, v69
	v_lshlrev_b32_e32 v32, 16, v32
	v_mul_f32_e32 v32, 0xbfb8aa3b, v32
	v_exp_f32_e32 v32, v32
	v_mul_f32_e32 v33, v33, v2
	v_add_f32_e32 v32, 1.0, v32
	v_rcp_f32_e32 v32, v32
	s_nop 0
	v_mul_f32_e32 v32, v33, v32
	v_cvt_pk_bf16_f32 v32, v32, s0
	ds_write_b16 v203, v32 offset:35040
	v_add_u32_e32 v32, -1, v7
	v_fma_f32 v33, -v32, v7, v3
	v_cmp_ge_f32_e64 s[0:1], 0, v33
	v_add_u32_e32 v33, 1, v7
	s_nop 0
	v_cndmask_b32_e64 v32, v7, v32, s[0:1]
	v_fma_f32 v7, -v33, v7, v3
	v_cmp_lt_f32_e64 s[0:1], 0, v7
	s_nop 1
; __device__ __forceinline__ float bf2f(bf16_t b) { return __uint_as_float(((unsigned)b) << 16); }
; __device__ __forceinline__ float sigmoidf_(float x) { return __builtin_amdgcn_rcpf(1.0f + __expf(-x)); }
; __device__ __forceinline__ bf16_t f2bf(float v) { return (bf16_t)(cvt_pk_bf16(v, 0.f) & 0xffffu); }
; __device__ __forceinline__ void ml_out_phase(const Params& p, Frame& F) {
;     ...
;         for (int i = 0; i < 4; ++i) { const int tl = 16 * tb + 4 * fq + i; const float r = 1.0f / sqrtf((ssqp[tl] + ssqp[64 + tl]) * (1.0f / 256.0f) + EPS);
; #pragma unroll
;             for (int nb = 0; nb < 8; ++nb) { const int v = 16 * (8 * vh + nb) + fr; const float g = bf2f(VR[tl * 256 + v]);
;                 VR[tl * 256 + v] = f2bf(o[nb][i] * r * nwl[v] * sigmoidf_(g)); } }
	v_cndmask_b32_e64 v7, v32, v33, s[0:1]
	v_mul_f32_e32 v32, 0x37800000, v7
	v_cndmask_b32_e32 v7, v7, v32, vcc
	v_cmp_class_f32_e32 vcc, v3, v222
	s_nop 1
	v_cndmask_b32_e32 v3, v7, v3, vcc
	v_div_scale_f32 v7, s[0:1], v3, v3, 1.0
	v_rcp_f32_e32 v32, v7
	s_nop 0
	v_fma_f32 v33, -v7, v32, 1.0
	v_fmac_f32_e32 v32, v33, v32
	v_div_scale_f32 v33, vcc, 1.0, v3, 1.0
	v_mul_f32_e32 v34, v33, v32
	v_fma_f32 v36, -v7, v34, v33
	v_fmac_f32_e32 v34, v36, v32
	v_fma_f32 v7, -v7, v34, v33
	v_div_fmas_f32 v7, v7, v32, v34
	v_div_fixup_f32 v3, v7, v3, 1.0
	v_mov_b32_e32 v7, v70
	v_mul_f32_e32 v32, v49, v3
	v_mul_f32_e32 v32, v20, v32
	v_lshlrev_b32_e32 v7, 16, v7
	v_mul_f32_e32 v7, 0xbfb8aa3b, v7
	v_exp_f32_e32 v7, v7
	s_nop 0
	v_add_f32_e32 v7, 1.0, v7
	v_rcp_f32_e32 v7, v7
	s_nop 0
	v_mul_f32_e32 v7, v32, v7
	v_cvt_pk_bf16_f32 v7, v7, s0
	ds_write_b16 v212, v7 offset:34816
	v_mov_b32_e32 v7, v71
	v_mul_f32_e32 v32, v47, v3
	v_mul_f32_e32 v32, v6, v32
	v_lshlrev_b32_e32 v7, 16, v7
	v_mul_f32_e32 v7, 0xbfb8aa3b, v7
	v_exp_f32_e32 v7, v7
	s_nop 0
	v_add_f32_e32 v7, 1.0, v7
	v_rcp_f32_e32 v7, v7
	s_nop 0
	v_mul_f32_e32 v7, v32, v7
	v_cvt_pk_bf16_f32 v7, v7, s0
	ds_write_b16 v212, v7 offset:34848
	v_mov_b32_e32 v7, v72
	v_mul_f32_e32 v32, v45, v3
	v_mul_f32_e32 v32, v21, v32
	v_lshlrev_b32_e32 v7, 16, v7
	v_mul_f32_e32 v7, 0xbfb8aa3b, v7
	v_exp_f32_e32 v7, v7
	s_nop 0
	v_add_f32_e32 v7, 1.0, v7
	v_rcp_f32_e32 v7, v7
	s_nop 0
	v_mul_f32_e32 v7, v32, v7
	v_cvt_pk_bf16_f32 v7, v7, s0
	ds_write_b16 v212, v7 offset:34880
	v_mov_b32_e32 v7, v73
	v_mul_f32_e32 v32, v43, v3
	v_mul_f32_e32 v32, v24, v32
	v_lshlrev_b32_e32 v7, 16, v7
	v_mul_f32_e32 v7, 0xbfb8aa3b, v7
	v_exp_f32_e32 v7, v7
	s_nop 0
	v_add_f32_e32 v7, 1.0, v7
	v_rcp_f32_e32 v7, v7
	s_nop 0
	v_mul_f32_e32 v7, v32, v7
	v_cvt_pk_bf16_f32 v7, v7, s0
	ds_write_b16 v212, v7 offset:34912
	v_mov_b32_e32 v7, v74
	v_mul_f32_e32 v32, v41, v3
	v_mul_f32_e32 v32, v25, v32
	v_lshlrev_b32_e32 v7, 16, v7
	v_mul_f32_e32 v7, 0xbfb8aa3b, v7
	v_exp_f32_e32 v7, v7
	s_nop 0
	v_add_f32_e32 v7, 1.0, v7
	v_rcp_f32_e32 v7, v7
	s_nop 0
	v_mul_f32_e32 v7, v32, v7
	v_cvt_pk_bf16_f32 v7, v7, s0
	ds_write_b16 v212, v7 offset:34944
	v_mov_b32_e32 v7, v75
	v_mul_f32_e32 v32, v39, v3
	v_mul_f32_e32 v32, v28, v32
	v_lshlrev_b32_e32 v7, 16, v7
	v_mul_f32_e32 v7, 0xbfb8aa3b, v7
	v_exp_f32_e32 v7, v7
	s_nop 0
	v_add_f32_e32 v7, 1.0, v7
	v_rcp_f32_e32 v7, v7
	s_nop 0
	v_mul_f32_e32 v7, v32, v7
	v_cvt_pk_bf16_f32 v7, v7, s0
	ds_write_b16 v212, v7 offset:34976
	v_mov_b32_e32 v7, v76
	v_mul_f32_e32 v32, v37, v3
	v_mul_f32_e32 v32, v29, v32
	v_mul_f32_e32 v3, v35, v3
	v_mul_f32_e32 v3, v2, v3
	v_lshlrev_b32_e32 v7, 16, v7
	v_mul_f32_e32 v7, 0xbfb8aa3b, v7
	v_exp_f32_e32 v7, v7
	s_nop 0
	v_add_f32_e32 v7, 1.0, v7
	v_rcp_f32_e32 v7, v7
	s_nop 0
	v_mul_f32_e32 v7, v32, v7
	v_cvt_pk_bf16_f32 v7, v7, s0
	ds_write_b16 v212, v7 offset:35008
	v_mov_b32_e32 v7, v77
	v_lshlrev_b32_e32 v7, 16, v7
	v_mul_f32_e32 v7, 0xbfb8aa3b, v7
	v_exp_f32_e32 v7, v7
	s_nop 0
	v_add_f32_e32 v7, 1.0, v7
	v_rcp_f32_e32 v7, v7
	s_nop 0
	v_mul_f32_e32 v3, v3, v7
	v_cvt_pk_bf16_f32 v3, v3, s0
	ds_write_b16 v212, v3 offset:35040
	v_add_f32_e32 v3, v4, v8
	v_fmamk_f32 v3, v3, 0x3b800000, v221
	v_cmp_gt_f32_e32 vcc, s11, v3
	v_mul_f32_e32 v4, 0x4f800000, v3
	s_nop 0
	v_cndmask_b32_e32 v3, v3, v4, vcc
	v_sqrt_f32_e32 v4, v3
	s_nop 0
	v_add_u32_e32 v7, -1, v4
	v_fma_f32 v8, -v7, v4, v3
	v_cmp_ge_f32_e64 s[0:1], 0, v8
	v_add_u32_e32 v8, 1, v4
	s_nop 0
	v_cndmask_b32_e64 v7, v4, v7, s[0:1]
	v_fma_f32 v4, -v8, v4, v3
	v_cmp_lt_f32_e64 s[0:1], 0, v4
	s_nop 1
	v_cndmask_b32_e64 v4, v7, v8, s[0:1]
	v_mul_f32_e32 v7, 0x37800000, v4
	v_cndmask_b32_e32 v4, v4, v7, vcc
	v_cmp_class_f32_e32 vcc, v3, v222
	s_nop 1
	v_cndmask_b32_e32 v3, v4, v3, vcc
	v_div_scale_f32 v4, s[0:1], v3, v3, 1.0
	v_rcp_f32_e32 v7, v4
	s_nop 0
	v_fma_f32 v8, -v4, v7, 1.0
	v_fmac_f32_e32 v7, v8, v7
	v_div_scale_f32 v8, vcc, 1.0, v3, 1.0
	v_mul_f32_e32 v32, v8, v7
	v_fma_f32 v33, -v4, v32, v8
	v_fmac_f32_e32 v32, v33, v7
	v_fma_f32 v4, -v4, v32, v8
	v_div_fmas_f32 v4, v4, v7, v32
	v_div_fixup_f32 v3, v4, v3, 1.0
	v_mov_b32_e32 v4, v78
	v_mul_f32_e32 v7, v30, v3
	v_mul_f32_e32 v7, v20, v7
	v_lshlrev_b32_e32 v4, 16, v4
	v_mul_f32_e32 v4, 0xbfb8aa3b, v4
	v_exp_f32_e32 v4, v4
	s_nop 0
	v_add_f32_e32 v4, 1.0, v4
	v_rcp_f32_e32 v4, v4
	s_nop 0
	v_mul_f32_e32 v4, v7, v4
	v_cvt_pk_bf16_f32 v4, v4, s0
	ds_write_b16 v213, v4 offset:34816
	v_mov_b32_e32 v4, v79
	v_mul_f32_e32 v7, v26, v3
	v_mul_f32_e32 v7, v6, v7
	v_lshlrev_b32_e32 v4, 16, v4
	v_mul_f32_e32 v4, 0xbfb8aa3b, v4
	v_exp_f32_e32 v4, v4
	s_nop 0
	v_add_f32_e32 v4, 1.0, v4
	v_rcp_f32_e32 v4, v4
	s_nop 0
	v_mul_f32_e32 v4, v7, v4
	v_cvt_pk_bf16_f32 v4, v4, s0
	ds_write_b16 v213, v4 offset:34848
	v_mov_b32_e32 v4, v80
	v_mul_f32_e32 v7, v22, v3
	v_mul_f32_e32 v7, v21, v7
	v_lshlrev_b32_e32 v4, 16, v4
	v_mul_f32_e32 v4, 0xbfb8aa3b, v4
	v_exp_f32_e32 v4, v4
	s_nop 0
	v_add_f32_e32 v4, 1.0, v4
	v_rcp_f32_e32 v4, v4
	s_nop 0
	v_mul_f32_e32 v4, v7, v4
	v_cvt_pk_bf16_f32 v4, v4, s0
	ds_write_b16 v213, v4 offset:34880
	v_mov_b32_e32 v4, v81
	v_mul_f32_e32 v7, v18, v3
	v_mul_f32_e32 v7, v24, v7
	v_lshlrev_b32_e32 v4, 16, v4
	v_mul_f32_e32 v4, 0xbfb8aa3b, v4
; __device__ __forceinline__ float bf2f(bf16_t b) { return __uint_as_float(((unsigned)b) << 16); }
; __device__ __forceinline__ float sigmoidf_(float x) { return __builtin_amdgcn_rcpf(1.0f + __expf(-x)); }
; #define LBAR() do { asm volatile("s_waitcnt lgkmcnt(0)" ::: "memory"); __builtin_amdgcn_s_barrier(); asm volatile("" ::: "memory"); } while (0)
; __device__ __forceinline__ bf16_t f2bf(float v) { return (bf16_t)(cvt_pk_bf16(v, 0.f) & 0xffffu); }
; __device__ __forceinline__ void ml_out_phase(const Params& p, Frame& F) {
;     ...
;         for (int i = 0; i < 4; ++i) { const int tl = 16 * tb + 4 * fq + i; const float r = 1.0f / sqrtf((ssqp[tl] + ssqp[64 + tl]) * (1.0f / 256.0f) + EPS);
; #pragma unroll
;             for (int nb = 0; nb < 8; ++nb) { const int v = 16 * (8 * vh + nb) + fr; const float g = bf2f(VR[tl * 256 + v]);
;                 VR[tl * 256 + v] = f2bf(o[nb][i] * r * nwl[v] * sigmoidf_(g)); } }
;         LBAR();
;         bf16_t* mix = (bf16_t*)(ws + WS_MIX) + t0 * DM + 1024 + h * 256;
	v_exp_f32_e32 v4, v4
	s_nop 0
	v_add_f32_e32 v4, 1.0, v4
	v_rcp_f32_e32 v4, v4
	s_nop 0
	v_mul_f32_e32 v4, v7, v4
	v_cvt_pk_bf16_f32 v4, v4, s0
	ds_write_b16 v213, v4 offset:34912
	v_mov_b32_e32 v4, v82
	v_mul_f32_e32 v7, v16, v3
	v_mul_f32_e32 v7, v25, v7
	v_lshlrev_b32_e32 v4, 16, v4
	v_mul_f32_e32 v4, 0xbfb8aa3b, v4
	v_exp_f32_e32 v4, v4
	s_nop 0
	v_add_f32_e32 v4, 1.0, v4
	v_rcp_f32_e32 v4, v4
	s_nop 0
	v_mul_f32_e32 v4, v7, v4
	v_cvt_pk_bf16_f32 v4, v4, s0
	ds_write_b16 v213, v4 offset:34944
	v_mov_b32_e32 v4, v83
	v_mul_f32_e32 v7, v14, v3
	v_mul_f32_e32 v7, v28, v7
	v_lshlrev_b32_e32 v4, 16, v4
	v_mul_f32_e32 v4, 0xbfb8aa3b, v4
	v_exp_f32_e32 v4, v4
	s_nop 0
	v_add_f32_e32 v4, 1.0, v4
	v_rcp_f32_e32 v4, v4
	s_nop 0
	v_mul_f32_e32 v4, v7, v4
	v_cvt_pk_bf16_f32 v4, v4, s0
	ds_write_b16 v213, v4 offset:34976
	v_mov_b32_e32 v4, v84
	v_mul_f32_e32 v7, v12, v3
	v_mul_f32_e32 v7, v29, v7
	v_mul_f32_e32 v3, v10, v3
	v_mul_f32_e32 v3, v2, v3
	v_lshlrev_b32_e32 v4, 16, v4
	v_mul_f32_e32 v4, 0xbfb8aa3b, v4
	v_exp_f32_e32 v4, v4
	s_nop 0
	v_add_f32_e32 v4, 1.0, v4
	v_rcp_f32_e32 v4, v4
	s_nop 0
	v_mul_f32_e32 v4, v7, v4
	v_cvt_pk_bf16_f32 v4, v4, s0
	ds_write_b16 v213, v4 offset:35008
	v_mov_b32_e32 v4, v85
	v_lshlrev_b32_e32 v4, 16, v4
	v_mul_f32_e32 v4, 0xbfb8aa3b, v4
	v_exp_f32_e32 v4, v4
	s_nop 0
	v_add_f32_e32 v4, 1.0, v4
	v_rcp_f32_e32 v4, v4
	s_nop 0
	v_mul_f32_e32 v3, v3, v4
	v_cvt_pk_bf16_f32 v3, v3, s0
	ds_write_b16 v213, v3 offset:35040
	v_add_f32_e32 v3, v5, v9
	v_fmamk_f32 v3, v3, 0x3b800000, v221
	v_cmp_gt_f32_e32 vcc, s11, v3
	v_mul_f32_e32 v4, 0x4f800000, v3
	s_nop 0
	v_cndmask_b32_e32 v3, v3, v4, vcc
	v_sqrt_f32_e32 v4, v3
	s_nop 0
	v_add_u32_e32 v5, -1, v4
	v_fma_f32 v7, -v5, v4, v3
	v_cmp_ge_f32_e64 s[0:1], 0, v7
	v_add_u32_e32 v7, 1, v4
	s_nop 0
	v_cndmask_b32_e64 v5, v4, v5, s[0:1]
	v_fma_f32 v4, -v7, v4, v3
	v_cmp_lt_f32_e64 s[0:1], 0, v4
	s_nop 1
	v_cndmask_b32_e64 v4, v5, v7, s[0:1]
	v_mul_f32_e32 v5, 0x37800000, v4
	v_cndmask_b32_e32 v4, v4, v5, vcc
	v_cmp_class_f32_e32 vcc, v3, v222
	s_nop 1
	v_cndmask_b32_e32 v3, v4, v3, vcc
	v_div_scale_f32 v4, s[0:1], v3, v3, 1.0
	v_rcp_f32_e32 v5, v4
	s_nop 0
	v_fma_f32 v7, -v4, v5, 1.0
	v_fmac_f32_e32 v5, v7, v5
	v_div_scale_f32 v7, vcc, 1.0, v3, 1.0
	v_mul_f32_e32 v8, v7, v5
	v_fma_f32 v9, -v4, v8, v7
	v_fmac_f32_e32 v8, v9, v5
	v_fma_f32 v4, -v4, v8, v7
	v_div_fmas_f32 v4, v4, v5, v8
	v_div_fixup_f32 v3, v4, v3, 1.0
	v_mov_b32_e32 v4, v86
	v_mul_f32_e32 v5, v31, v3
	v_mul_f32_e32 v5, v20, v5
	v_lshlrev_b32_e32 v4, 16, v4
	v_mul_f32_e32 v4, 0xbfb8aa3b, v4
	v_exp_f32_e32 v4, v4
	s_nop 0
	v_add_f32_e32 v4, 1.0, v4
	v_rcp_f32_e32 v4, v4
	s_nop 0
	v_mul_f32_e32 v4, v5, v4
	v_cvt_pk_bf16_f32 v4, v4, s0
	ds_write_b16 v214, v4 offset:34816
	v_mov_b32_e32 v4, v87
	v_mul_f32_e32 v5, v27, v3
	v_mul_f32_e32 v5, v6, v5
	v_lshlrev_b32_e32 v4, 16, v4
	v_mul_f32_e32 v4, 0xbfb8aa3b, v4
	v_exp_f32_e32 v4, v4
	s_nop 0
	v_add_f32_e32 v4, 1.0, v4
	v_rcp_f32_e32 v4, v4
	s_nop 0
	v_mul_f32_e32 v4, v5, v4
	v_cvt_pk_bf16_f32 v4, v4, s0
	ds_write_b16 v214, v4 offset:34848
	v_mov_b32_e32 v4, v88
	v_mul_f32_e32 v5, v23, v3
	v_mul_f32_e32 v5, v21, v5
	v_lshlrev_b32_e32 v4, 16, v4
	v_mul_f32_e32 v4, 0xbfb8aa3b, v4
	v_exp_f32_e32 v4, v4
	s_nop 0
	v_add_f32_e32 v4, 1.0, v4
	v_rcp_f32_e32 v4, v4
	s_nop 0
	v_mul_f32_e32 v4, v5, v4
	v_cvt_pk_bf16_f32 v4, v4, s0
	ds_write_b16 v214, v4 offset:34880
	v_mov_b32_e32 v4, v89
	v_mul_f32_e32 v5, v19, v3
	v_mul_f32_e32 v5, v24, v5
	v_lshlrev_b32_e32 v4, 16, v4
	v_mul_f32_e32 v4, 0xbfb8aa3b, v4
	v_exp_f32_e32 v4, v4
	s_nop 0
	v_add_f32_e32 v4, 1.0, v4
	v_rcp_f32_e32 v4, v4
	s_nop 0
	v_mul_f32_e32 v4, v5, v4
	v_cvt_pk_bf16_f32 v4, v4, s0
	ds_write_b16 v214, v4 offset:34912
	v_mov_b32_e32 v4, v90
	v_mul_f32_e32 v5, v17, v3
	v_mul_f32_e32 v5, v25, v5
	v_lshlrev_b32_e32 v4, 16, v4
	v_mul_f32_e32 v4, 0xbfb8aa3b, v4
	v_exp_f32_e32 v4, v4
	s_nop 0
	v_add_f32_e32 v4, 1.0, v4
	v_rcp_f32_e32 v4, v4
	s_nop 0
	v_mul_f32_e32 v4, v5, v4
	v_cvt_pk_bf16_f32 v4, v4, s0
	ds_write_b16 v214, v4 offset:34944
	v_mov_b32_e32 v4, v91
	v_mul_f32_e32 v5, v15, v3
	v_mul_f32_e32 v5, v28, v5
	v_lshlrev_b32_e32 v4, 16, v4
	v_mul_f32_e32 v4, 0xbfb8aa3b, v4
	v_exp_f32_e32 v4, v4
	s_nop 0
	v_add_f32_e32 v4, 1.0, v4
	v_rcp_f32_e32 v4, v4
	s_nop 0
	v_mul_f32_e32 v4, v5, v4
	v_cvt_pk_bf16_f32 v4, v4, s0
	ds_write_b16 v214, v4 offset:34976
	v_mov_b32_e32 v4, v92
	v_mul_f32_e32 v5, v13, v3
	v_mul_f32_e32 v5, v29, v5
	v_mul_f32_e32 v3, v11, v3
	v_mul_f32_e32 v2, v2, v3
	v_lshlrev_b32_e32 v4, 16, v4
	v_mul_f32_e32 v4, 0xbfb8aa3b, v4
	v_exp_f32_e32 v4, v4
	s_nop 0
	v_add_f32_e32 v4, 1.0, v4
	v_rcp_f32_e32 v4, v4
	s_nop 0
	v_mul_f32_e32 v4, v5, v4
	v_cvt_pk_bf16_f32 v4, v4, s0
	ds_write_b16 v214, v4 offset:35008
	v_mov_b32_e32 v4, v93
	v_mov_b32_e32 v5, v215
	v_lshlrev_b32_e32 v4, 16, v4
	v_mul_f32_e32 v3, 0xbfb8aa3b, v4
	v_exp_f32_e32 v3, v3
	v_mov_b32_e32 v4, v216
	v_add_f32_e32 v3, 1.0, v3
	v_rcp_f32_e32 v3, v3
	s_nop 0
	v_mul_f32_e32 v2, v2, v3
	v_cvt_pk_bf16_f32 v2, v2, s0
	ds_write_b16 v214, v2 offset:35040
	s_lshl_b64 s[0:1], s[74:75], 25
	s_waitcnt lgkmcnt(0)
	s_barrier
	s_or_b32 s0, s0, s58
	s_or_b64 s[0:1], s[0:1], s[22:23]
	v_lshl_add_u64 v[2:3], v[150:151], 0, s[0:1]
	s_mov_b64 s[0:1], 0
